# s11 + s_setprio 1 for waves that actually mask a band tile (until that tile's barrier), 4 main-loop sites
# speedup vs baseline: 1.0058x; 1.0029x over previous
; __device__ __forceinline__ void cmask(f32x16& p0, f32x16& p1, int jb, int qrel, int hi) {
;     const float NEG = -INFINITY; int kb = 64 * jb + 4 * hi;
; #pragma unroll
;     for (int r = 0; r < 16; ++r) { int kv = kb + (r & 3) + 8 * (r >> 2); if (kv > qrel) p0[r] = NEG; if (kv + 32 > qrel) p1[r] = NEG; }
; }
.LBB0_477:
	v_add_u32_e32 v184, s0, v230
	ds_read_b64_tr_b16 v[180:181], v184 offset:24576
	ds_read_b64_tr_b16 v[182:183], v184 offset:25088
	s_waitcnt lgkmcnt(9)
	v_mfma_f32_32x32x16_f16 v[48:63], v[176:179], v[128:131], v[48:63]
	v_add_f32_e32 v132, v80, v81
	v_add_f32_e32 v132, v82, v132
	v_add_f32_e32 v132, v83, v132
	v_add_f32_e32 v132, v84, v132
	v_add_f32_e32 v132, v85, v132
	v_cvt_pk_f16_f32 v144, v80, v81
	v_cvt_pk_f16_f32 v145, v82, v83
	ds_read_b64_tr_b16 v[176:177], v184 offset:28672
	ds_read_b64_tr_b16 v[178:179], v184 offset:29184
	s_waitcnt lgkmcnt(10)
	v_mfma_f32_32x32x16_f16 v[32:47], v[172:175], v[128:131], v[32:47]
	v_add_f32_e32 v80, v86, v132
	v_add_f32_e32 v80, v87, v80
	v_add_f32_e32 v80, v88, v80
	v_add_f32_e32 v80, v89, v80
	v_cvt_pk_f16_f32 v146, v84, v85
	v_cvt_pk_f16_f32 v147, v86, v87
	ds_read_b64_tr_b16 v[172:173], v184 offset:25600
	ds_read_b64_tr_b16 v[174:175], v184 offset:26112
	s_waitcnt lgkmcnt(11)
	v_mfma_f32_32x32x16_f16 v[48:63], v[168:171], v[124:127], v[48:63]
	v_add_f32_e32 v80, v90, v80
	v_add_f32_e32 v80, v91, v80
	v_add_f32_e32 v80, v92, v80
	v_add_f32_e32 v80, v93, v80
	v_cvt_pk_f16_f32 v140, v88, v89
	v_cvt_pk_f16_f32 v141, v90, v91
	ds_read_b64_tr_b16 v[84:85], v184 offset:29696
	ds_read_b64_tr_b16 v[86:87], v184 offset:30208
	s_waitcnt lgkmcnt(12)
	v_mfma_f32_32x32x16_f16 v[32:47], v[164:167], v[124:127], v[32:47]
	v_add_f32_e32 v80, v94, v80
	v_add_f32_e32 v80, v95, v80
	v_add_f32_e32 v80, v64, v80
	v_add_f32_e32 v88, v65, v80
	v_cvt_pk_f16_f32 v142, v92, v93
	v_cvt_pk_f16_f32 v143, v94, v95
	ds_read_b64_tr_b16 v[80:81], v184 offset:26624
	ds_read_b64_tr_b16 v[82:83], v184 offset:27136
	s_waitcnt lgkmcnt(13)
	v_mfma_f32_32x32x16_f16 v[48:63], v[160:163], v[120:123], v[48:63]
	v_add_f32_e32 v88, v66, v88
	v_add_f32_e32 v88, v67, v88
	v_add_f32_e32 v88, v68, v88
	v_add_f32_e32 v88, v69, v88
	v_cvt_pk_f16_f32 v136, v64, v65
	v_cvt_pk_f16_f32 v137, v66, v67
	ds_read_b64_tr_b16 v[160:161], v184 offset:30720
	ds_read_b64_tr_b16 v[162:163], v184 offset:31232
	s_waitcnt lgkmcnt(14)
	v_mfma_f32_32x32x16_f16 v[32:47], v[152:155], v[120:123], v[32:47]
	v_add_f32_e32 v64, v70, v88
	v_add_f32_e32 v64, v71, v64
	v_add_f32_e32 v64, v72, v64
	v_add_f32_e32 v88, v73, v64
	v_cvt_pk_f16_f32 v138, v68, v69
	v_cvt_pk_f16_f32 v139, v70, v71
	ds_read_b64_tr_b16 v[64:65], v184 offset:27648
	ds_read_b64_tr_b16 v[66:67], v184 offset:28160
	s_waitcnt lgkmcnt(14)
	v_mfma_f32_32x32x16_f16 v[48:63], v[156:159], v[116:119], v[48:63]
	v_add_f32_e32 v68, v74, v88
	v_add_f32_e32 v68, v75, v68
	v_add_f32_e32 v68, v76, v68
	v_add_f32_e32 v68, v77, v68
	v_cvt_pk_f16_f32 v132, v72, v73
	v_cvt_pk_f16_f32 v133, v74, v75
	ds_read_b64_tr_b16 v[152:153], v184 offset:31744
	ds_read_b64_tr_b16 v[154:155], v184 offset:32256
	v_mfma_f32_32x32x16_f16 v[32:47], v[148:151], v[116:119], v[32:47]
	v_add_f32_e32 v68, v78, v68
	v_add_f32_e32 v68, v79, v68
	v_add_f32_e32 v68, 0, v68
	v_cvt_pk_f16_f32 v134, v76, v77
	v_cvt_pk_f16_f32 v135, v78, v79
	s_add_i32 s0, s70, s89
	s_cmp_lt_u32 s69, 3
	s_cselect_b64 s[40:41], -1, 0
	s_mov_b32 s1, m0
	s_mov_b32 m0, s0
	s_nop 0
	global_load_lds_dwordx4 v[194:195], off
	s_mov_b32 m0, s1
	s_and_b64 s[0:1], s[40:41], exec
	s_cselect_b32 s18, s50, -3
	s_add_i32 s18, s18, s69
	v_mad_i64_i32 v[70:71], s[0:1], s18, v249, v[216:217]
	s_add_i32 s0, s68, s36
	s_mov_b32 s1, m0
	s_mov_b32 m0, s0
	s_nop 0
	global_load_lds_dwordx4 v[70:71], off
	s_mov_b32 m0, s1
	s_cmp_gt_u32 s69, 3
	s_cbranch_scc1 .LBB0_479
	s_mov_b64 s[100:101], exec
	v_sub_u32_e32 v70, v215, v197
	v_add_u32_e32 v70, 0x7b, v70
	v_cmpx_gt_i32_e32 59, v70
	s_nop 3
	s_cbranch_execz .Lmaskx_done_9
	s_setprio 1
	v_mov_b32_e32 v47, v248
	v_cmpx_gt_i32_e32 58, v70
	v_mov_b32_e32 v46, v248
	v_cmpx_gt_i32_e32 57, v70
	v_mov_b32_e32 v45, v248
	v_cmpx_gt_i32_e32 56, v70
	v_mov_b32_e32 v44, v248
	v_cmpx_gt_i32_e32 51, v70
	v_mov_b32_e32 v43, v248
	v_cmpx_gt_i32_e32 50, v70
	v_mov_b32_e32 v42, v248
	v_cmpx_gt_i32_e32 49, v70
	v_mov_b32_e32 v41, v248
	v_cmpx_gt_i32_e32 48, v70
	v_mov_b32_e32 v40, v248
	v_cmpx_gt_i32_e32 43, v70
	v_mov_b32_e32 v39, v248
	v_cmpx_gt_i32_e32 42, v70
	v_mov_b32_e32 v38, v248
	v_cmpx_gt_i32_e32 41, v70
	v_mov_b32_e32 v37, v248
	v_cmpx_gt_i32_e32 40, v70
	v_mov_b32_e32 v36, v248
	v_cmpx_gt_i32_e32 35, v70
	v_mov_b32_e32 v35, v248
	v_cmpx_gt_i32_e32 34, v70
	v_mov_b32_e32 v34, v248
	v_cmpx_gt_i32_e32 33, v70
	v_mov_b32_e32 v33, v248
	v_cmpx_gt_i32_e32 32, v70
	v_mov_b32_e32 v32, v248
	v_cmpx_gt_i32_e32 27, v70
	v_mov_b32_e32 v63, v248
	v_cmpx_gt_i32_e32 26, v70
	v_mov_b32_e32 v62, v248
	v_cmpx_gt_i32_e32 25, v70
	v_mov_b32_e32 v61, v248
	v_cmpx_gt_i32_e32 24, v70
	v_mov_b32_e32 v60, v248
	v_cmpx_gt_i32_e32 19, v70
	v_mov_b32_e32 v59, v248
	v_cmpx_gt_i32_e32 18, v70
	v_mov_b32_e32 v58, v248
	v_cmpx_gt_i32_e32 17, v70
	v_mov_b32_e32 v57, v248
	v_cmpx_gt_i32_e32 16, v70
	v_mov_b32_e32 v56, v248
	v_cmpx_gt_i32_e32 11, v70
	v_mov_b32_e32 v55, v248
	v_cmpx_gt_i32_e32 10, v70
	v_mov_b32_e32 v54, v248
	v_cmpx_gt_i32_e32 9, v70
	v_mov_b32_e32 v53, v248
	v_cmpx_gt_i32_e32 8, v70
	v_mov_b32_e32 v52, v248
	v_cmpx_gt_i32_e32 3, v70
	v_mov_b32_e32 v51, v248
	v_cmpx_gt_i32_e32 2, v70
	v_mov_b32_e32 v50, v248
	v_cmpx_gt_i32_e32 1, v70
	v_mov_b32_e32 v49, v248
	v_cmpx_gt_i32_e32 0, v70
	v_mov_b32_e32 v48, v248

; #define WAIT_BAR(N) asm volatile("s_waitcnt vmcnt(" #N ") lgkmcnt(0)\n\ts_barrier" ::: "memory")
; #define RESC() do { if (resc) { asm volatile("s_waitcnt lgkmcnt(0)" ::: "memory"); \
;       _Pragma("unroll") for (int d_ = 0; d_ < 2; ++d_) _Pragma("unroll") for (int r = 0; r < 16; ++r) o[d_][r] *= wsf[crow(r, hi)]; } } while (0)
; #define ROT() do { sl_prev = sl_cur; sl_cur = sl_next; sl_next = (sl_next == (NSLOT - 1) * SLOTB) ? 0 : sl_next + SLOTB; } while (0)
; template <bool MOBA, int THRL> ...
;     ...
;     int t = 1;
;     ...
;     for (; t + 5 < NT; t += 2) {
;         STEP(pB0, pB1, pA0, pA1, t, true, true, true);       WAIT_BAR(2); RESC(); ROT();
.LBB0_480:
	v_lshl_add_u32 v68, s18, 8, v234
	s_ashr_i32 s18, s18, 2
	v_bfe_u32 v69, v231, s18, 1
	v_cmp_eq_u32_e32 vcc, 0, v69
	s_nop 1
	v_cndmask_b32_e32 v69, v68, v196, vcc
	v_cndmask_b32_e64 v76, v69, v68, s[40:41]
	s_waitcnt lgkmcnt(14)
	v_mfma_f32_32x32x16_f16 v[16:31], v[144:147], v[180:183], v[16:31]
	v_exp_f32_e32 v48, v48
	v_exp_f32_e32 v49, v49
	v_exp_f32_e32 v50, v50
	v_exp_f32_e32 v51, v51
	ds_read_b128 v[156:159], v76
	ds_read_b128 v[68:71], v76 offset:128
	s_waitcnt lgkmcnt(14)
	v_mfma_f32_32x32x16_f16 v[0:15], v[144:147], v[176:179], v[0:15]
	v_exp_f32_e32 v52, v52
	v_exp_f32_e32 v53, v53
	v_exp_f32_e32 v54, v54
	v_exp_f32_e32 v55, v55
	ds_read_b128 v[168:171], v76 offset:32
	ds_read_b128 v[200:203], v76 offset:160
	v_add_u32_e32 v144, s68, v232
	ds_read_b128 v[188:191], v144
	ds_read_b128 v[148:151], v144 offset:512
	s_waitcnt lgkmcnt(14)
	v_mfma_f32_32x32x16_f16 v[16:31], v[140:143], v[172:175], v[16:31]
	v_exp_f32_e32 v56, v56
	v_exp_f32_e32 v57, v57
	v_exp_f32_e32 v58, v58
	v_exp_f32_e32 v59, v59
	ds_read_b128 v[88:91], v76 offset:64
	ds_read_b128 v[72:75], v76 offset:192
	ds_read_b128 v[184:187], v144 offset:2048
	ds_read_b128 v[172:175], v144 offset:2560
	v_mfma_f32_32x32x16_f16 v[0:15], v[140:143], v[84:87], v[0:15]
	v_exp_f32_e32 v60, v60
	v_exp_f32_e32 v61, v61
	v_exp_f32_e32 v62, v62
	v_exp_f32_e32 v63, v63
	ds_read_b128 v[92:95], v76 offset:96
	ds_read_b128 v[76:79], v76 offset:224
	ds_read_b128 v[176:179], v144 offset:4096
	ds_read_b128 v[164:167], v144 offset:4608
	s_waitcnt lgkmcnt(14)
	v_mfma_f32_32x32x16_f16 v[16:31], v[136:139], v[80:83], v[16:31]
	v_exp_f32_e32 v32, v32
	v_exp_f32_e32 v33, v33
	v_exp_f32_e32 v34, v34
	v_exp_f32_e32 v35, v35
	s_waitcnt lgkmcnt(13)
	v_pk_add_f32 v[80:81], v[156:157], v[218:219] op_sel_hi:[1,0] neg_lo:[0,1] neg_hi:[0,1]
	v_pk_add_f32 v[82:83], v[158:159], v[218:219] op_sel_hi:[1,0] neg_lo:[0,1] neg_hi:[0,1]
	s_waitcnt lgkmcnt(11)
	v_pk_add_f32 v[84:85], v[168:169], v[218:219] op_sel_hi:[1,0] neg_lo:[0,1] neg_hi:[0,1]
	v_pk_add_f32 v[86:87], v[170:171], v[218:219] op_sel_hi:[1,0] neg_lo:[0,1] neg_hi:[0,1]
	s_waitcnt lgkmcnt(3)
	ds_read_b128 v[180:183], v144 offset:6144
	ds_read_b128 v[168:171], v144 offset:6656
	v_mfma_f32_32x32x16_f16 v[0:15], v[136:139], v[160:163], v[0:15]
	v_exp_f32_e32 v36, v36
	v_exp_f32_e32 v37, v37
	v_exp_f32_e32 v38, v38
	v_exp_f32_e32 v39, v39
	v_pk_add_f32 v[88:89], v[88:89], v[218:219] op_sel_hi:[1,0] neg_lo:[0,1] neg_hi:[0,1]
	v_pk_add_f32 v[90:91], v[90:91], v[218:219] op_sel_hi:[1,0] neg_lo:[0,1] neg_hi:[0,1]
	v_pk_add_f32 v[92:93], v[92:93], v[218:219] op_sel_hi:[1,0] neg_lo:[0,1] neg_hi:[0,1]
	v_pk_add_f32 v[94:95], v[94:95], v[218:219] op_sel_hi:[1,0] neg_lo:[0,1] neg_hi:[0,1]
	s_nop 0
	v_mfma_f32_32x32x16_f16 v[16:31], v[132:135], v[64:67], v[16:31]
	v_exp_f32_e32 v40, v40
	v_exp_f32_e32 v41, v41
	v_exp_f32_e32 v42, v42
	v_exp_f32_e32 v43, v43
	v_pk_add_f32 v[64:65], v[68:69], v[218:219] op_sel_hi:[1,0] neg_lo:[0,1] neg_hi:[0,1]
	v_pk_add_f32 v[66:67], v[70:71], v[218:219] op_sel_hi:[1,0] neg_lo:[0,1] neg_hi:[0,1]
	v_pk_add_f32 v[68:69], v[200:201], v[218:219] op_sel_hi:[1,0] neg_lo:[0,1] neg_hi:[0,1]
	v_pk_add_f32 v[70:71], v[202:203], v[218:219] op_sel_hi:[1,0] neg_lo:[0,1] neg_hi:[0,1]
	s_waitcnt lgkmcnt(4)
	v_mfma_f32_32x32x16_f16 v[0:15], v[132:135], v[152:155], v[0:15]
	v_exp_f32_e32 v44, v44
	v_exp_f32_e32 v45, v45
	v_exp_f32_e32 v46, v46
	v_exp_f32_e32 v47, v47
	v_pk_add_f32 v[72:73], v[72:73], v[218:219] op_sel_hi:[1,0] neg_lo:[0,1] neg_hi:[0,1]
	v_pk_add_f32 v[74:75], v[74:75], v[218:219] op_sel_hi:[1,0] neg_lo:[0,1] neg_hi:[0,1]
	v_pk_add_f32 v[76:77], v[76:77], v[218:219] op_sel_hi:[1,0] neg_lo:[0,1] neg_hi:[0,1]
	v_pk_add_f32 v[78:79], v[78:79], v[218:219] op_sel_hi:[1,0] neg_lo:[0,1] neg_hi:[0,1]
	s_nop 0
	s_waitcnt vmcnt(2) lgkmcnt(0)
	s_barrier
	s_setprio 0
	s_andn2_b64 vcc, exec, s[0:1]
	s_cbranch_vccnz .LBB0_482
	s_waitcnt lgkmcnt(0)
	ds_read_b128 v[152:155], v228 offset:49248
	ds_read_b128 v[156:159], v228 offset:49216
	ds_read_b128 v[160:163], v228 offset:49184
	ds_read_b128 v[200:203], v228 offset:49152
	s_waitcnt lgkmcnt(3)
	v_pk_mul_f32 v[30:31], v[30:31], v[154:155]
	s_waitcnt lgkmcnt(2)
	v_pk_mul_f32 v[26:27], v[26:27], v[158:159]
	s_waitcnt lgkmcnt(1)
	v_pk_mul_f32 v[22:23], v[22:23], v[162:163]
	s_waitcnt lgkmcnt(0)
	v_pk_mul_f32 v[18:19], v[18:19], v[202:203]
	v_pk_mul_f32 v[28:29], v[28:29], v[152:153]
	v_pk_mul_f32 v[24:25], v[24:25], v[156:157]
	v_pk_mul_f32 v[20:21], v[20:21], v[160:161]
	v_pk_mul_f32 v[16:17], v[16:17], v[200:201]
	v_pk_mul_f32 v[14:15], v[14:15], v[154:155]
	v_pk_mul_f32 v[10:11], v[10:11], v[158:159]
	v_pk_mul_f32 v[6:7], v[6:7], v[162:163]
	v_pk_mul_f32 v[2:3], v[2:3], v[202:203]
	v_pk_mul_f32 v[12:13], v[12:13], v[152:153]
	v_pk_mul_f32 v[8:9], v[8:9], v[156:157]
	v_pk_mul_f32 v[4:5], v[4:5], v[160:161]
	v_pk_mul_f32 v[0:1], v[0:1], v[200:201]
; __device__ __forceinline__ void cmask(f32x16& p0, f32x16& p1, int jb, int qrel, int hi) {
;     const float NEG = -INFINITY; int kb = 64 * jb + 4 * hi;
; #pragma unroll
;     for (int r = 0; r < 16; ++r) { int kv = kb + (r & 3) + 8 * (r >> 2); if (kv > qrel) p0[r] = NEG; if (kv + 32 > qrel) p1[r] = NEG; }
; }
.LBB0_482:
	s_add_i32 s0, s68, 0x2000
	s_cmpk_lg_i32 s68, 0x4000
	s_cselect_b32 s45, s0, 0
	v_add_u32_e32 v160, s70, v230
	ds_read_b64_tr_b16 v[156:157], v160 offset:24576
	ds_read_b64_tr_b16 v[158:159], v160 offset:25088
	v_mfma_f32_32x32x16_f16 v[80:95], v[188:191], v[128:131], v[80:95]
	v_add_f32_e32 v132, v48, v49
	v_add_f32_e32 v132, v50, v132
	v_add_f32_e32 v132, v51, v132
	v_add_f32_e32 v132, v52, v132
	v_add_f32_e32 v132, v53, v132
	v_cvt_pk_f16_f32 v144, v48, v49
	v_cvt_pk_f16_f32 v145, v50, v51
	ds_read_b64_tr_b16 v[152:153], v160 offset:28672
	ds_read_b64_tr_b16 v[154:155], v160 offset:29184
	v_mfma_f32_32x32x16_f16 v[64:79], v[148:151], v[128:131], v[64:79]
	v_add_f32_e32 v48, v54, v132
	v_add_f32_e32 v48, v55, v48
	v_add_f32_e32 v48, v56, v48
	v_add_f32_e32 v48, v57, v48
	v_cvt_pk_f16_f32 v146, v52, v53
	v_cvt_pk_f16_f32 v147, v54, v55
	ds_read_b64_tr_b16 v[148:149], v160 offset:25600
	ds_read_b64_tr_b16 v[150:151], v160 offset:26112
	v_mfma_f32_32x32x16_f16 v[80:95], v[184:187], v[124:127], v[80:95]
	v_add_f32_e32 v48, v58, v48
	v_add_f32_e32 v48, v59, v48
	v_add_f32_e32 v48, v60, v48
	v_add_f32_e32 v48, v61, v48
	v_cvt_pk_f16_f32 v140, v56, v57
	v_cvt_pk_f16_f32 v141, v58, v59
	ds_read_b64_tr_b16 v[52:53], v160 offset:29696
	ds_read_b64_tr_b16 v[54:55], v160 offset:30208
	v_mfma_f32_32x32x16_f16 v[64:79], v[172:175], v[124:127], v[64:79]
	v_add_f32_e32 v48, v62, v48
	v_add_f32_e32 v48, v63, v48
	v_add_f32_e32 v48, v32, v48
	v_add_f32_e32 v56, v33, v48
	v_cvt_pk_f16_f32 v142, v60, v61
	v_cvt_pk_f16_f32 v143, v62, v63
	ds_read_b64_tr_b16 v[48:49], v160 offset:26624
	ds_read_b64_tr_b16 v[50:51], v160 offset:27136
	s_waitcnt lgkmcnt(13)
	v_mfma_f32_32x32x16_f16 v[80:95], v[176:179], v[120:123], v[80:95]
	v_add_f32_e32 v56, v34, v56
	v_add_f32_e32 v56, v35, v56
	v_add_f32_e32 v56, v36, v56
	v_add_f32_e32 v56, v37, v56
	v_cvt_pk_f16_f32 v136, v32, v33
	v_cvt_pk_f16_f32 v137, v34, v35
	ds_read_b64_tr_b16 v[184:185], v160 offset:30720
	ds_read_b64_tr_b16 v[186:187], v160 offset:31232
	s_waitcnt lgkmcnt(14)
	v_mfma_f32_32x32x16_f16 v[64:79], v[164:167], v[120:123], v[64:79]
	v_add_f32_e32 v32, v38, v56
	v_add_f32_e32 v32, v39, v32
	v_add_f32_e32 v32, v40, v32
	v_add_f32_e32 v56, v41, v32
	v_cvt_pk_f16_f32 v138, v36, v37
	v_cvt_pk_f16_f32 v139, v38, v39
	ds_read_b64_tr_b16 v[32:33], v160 offset:27648
	ds_read_b64_tr_b16 v[34:35], v160 offset:28160
	s_waitcnt lgkmcnt(14)
	v_mfma_f32_32x32x16_f16 v[80:95], v[180:183], v[116:119], v[80:95]
	v_add_f32_e32 v36, v42, v56
	v_add_f32_e32 v36, v43, v36
	v_add_f32_e32 v36, v44, v36
	v_add_f32_e32 v36, v45, v36
	v_cvt_pk_f16_f32 v132, v40, v41
	v_cvt_pk_f16_f32 v133, v42, v43
	ds_read_b64_tr_b16 v[180:181], v160 offset:31744
	ds_read_b64_tr_b16 v[182:183], v160 offset:32256
	v_mfma_f32_32x32x16_f16 v[64:79], v[168:171], v[116:119], v[64:79]
	v_add_f32_e32 v36, v46, v36
	v_add_f32_e32 v36, v47, v36
	v_add_f32_e32 v36, 0, v36
	v_cvt_pk_f16_f32 v134, v44, v45
	v_cvt_pk_f16_f32 v135, v46, v47
	s_add_i32 s0, s68, s89
	v_lshl_add_u64 v[38:39], v[194:195], 0, s[30:31]
	s_mov_b32 s1, m0
	s_mov_b32 m0, s0
	s_nop 0
	global_load_lds_dwordx4 v[38:39], off
	s_mov_b32 m0, s1
	s_cmp_lt_u32 s69, 2
	s_cselect_b64 s[0:1], -1, 0
	s_and_b64 s[18:19], s[0:1], exec
	s_cselect_b32 s18, s51, -2
	s_add_i32 s18, s18, s69
	v_mad_i64_i32 v[38:39], s[46:47], s18, v249, v[216:217]
	s_add_i32 s19, s45, s36
	s_mov_b32 s46, m0
	s_mov_b32 m0, s19
	s_nop 0
	global_load_lds_dwordx4 v[38:39], off
	s_mov_b32 m0, s46
	s_andn2_b64 vcc, exec, s[40:41]
	s_cbranch_vccnz .LBB0_484
	s_mov_b64 s[100:101], exec
	v_sub_u32_e32 v38, v215, v197
	v_add_u32_e32 v38, 59, v38
	v_cmpx_gt_i32_e32 59, v38
	s_nop 3
	s_cbranch_execz .Lmaskx_done_8
	s_setprio 1
	v_mov_b32_e32 v79, v248
	v_cmpx_gt_i32_e32 58, v38
	v_mov_b32_e32 v78, v248
	v_cmpx_gt_i32_e32 57, v38
	v_mov_b32_e32 v77, v248
	v_cmpx_gt_i32_e32 56, v38
	v_mov_b32_e32 v76, v248
	v_cmpx_gt_i32_e32 51, v38
	v_mov_b32_e32 v75, v248
	v_cmpx_gt_i32_e32 50, v38
	v_mov_b32_e32 v74, v248
	v_cmpx_gt_i32_e32 49, v38
	v_mov_b32_e32 v73, v248
	v_cmpx_gt_i32_e32 48, v38
	v_mov_b32_e32 v72, v248
	v_cmpx_gt_i32_e32 43, v38
	v_mov_b32_e32 v71, v248
	v_cmpx_gt_i32_e32 42, v38
	v_mov_b32_e32 v70, v248
	v_cmpx_gt_i32_e32 41, v38
	v_mov_b32_e32 v69, v248
	v_cmpx_gt_i32_e32 40, v38
	v_mov_b32_e32 v68, v248
	v_cmpx_gt_i32_e32 35, v38
	v_mov_b32_e32 v67, v248
	v_cmpx_gt_i32_e32 34, v38
	v_mov_b32_e32 v66, v248
	v_cmpx_gt_i32_e32 33, v38
	v_mov_b32_e32 v65, v248
	v_cmpx_gt_i32_e32 32, v38
	v_mov_b32_e32 v64, v248
	v_cmpx_gt_i32_e32 27, v38
	v_mov_b32_e32 v95, v248
	v_cmpx_gt_i32_e32 26, v38
	v_mov_b32_e32 v94, v248
	v_cmpx_gt_i32_e32 25, v38
	v_mov_b32_e32 v93, v248
	v_cmpx_gt_i32_e32 24, v38
	v_mov_b32_e32 v92, v248
	v_cmpx_gt_i32_e32 19, v38
	v_mov_b32_e32 v91, v248
	v_cmpx_gt_i32_e32 18, v38
	v_mov_b32_e32 v90, v248
	v_cmpx_gt_i32_e32 17, v38
	v_mov_b32_e32 v89, v248
	v_cmpx_gt_i32_e32 16, v38
	v_mov_b32_e32 v88, v248
	v_cmpx_gt_i32_e32 11, v38
	v_mov_b32_e32 v87, v248
	v_cmpx_gt_i32_e32 10, v38
	v_mov_b32_e32 v86, v248
	v_cmpx_gt_i32_e32 9, v38
	v_mov_b32_e32 v85, v248
	v_cmpx_gt_i32_e32 8, v38
	v_mov_b32_e32 v84, v248
	v_cmpx_gt_i32_e32 3, v38
	v_mov_b32_e32 v83, v248
	v_cmpx_gt_i32_e32 2, v38
	v_mov_b32_e32 v82, v248
	v_cmpx_gt_i32_e32 1, v38
	v_mov_b32_e32 v81, v248
	v_cmpx_gt_i32_e32 0, v38
	v_mov_b32_e32 v80, v248

; #define WAIT_BAR(N) asm volatile("s_waitcnt vmcnt(" #N ") lgkmcnt(0)\n\ts_barrier" ::: "memory")
; #define RESC() do { if (resc) { asm volatile("s_waitcnt lgkmcnt(0)" ::: "memory"); \
;       _Pragma("unroll") for (int d_ = 0; d_ < 2; ++d_) _Pragma("unroll") for (int r = 0; r < 16; ++r) o[d_][r] *= wsf[crow(r, hi)]; } } while (0)
; #define ROT() do { sl_prev = sl_cur; sl_cur = sl_next; sl_next = (sl_next == (NSLOT - 1) * SLOTB) ? 0 : sl_next + SLOTB; } while (0)
; template <bool MOBA, int THRL> ...
;     ...
;     bool resc = false;
;     ...
;     int t = 1;
;     ...
;     for (; t + 5 < NT; t += 2) {
;         STEP(pB0, pB1, pA0, pA1, t, true, true, true);       WAIT_BAR(2); RESC(); ROT();
.LBB0_485:
	v_lshl_add_u32 v36, s18, 8, v234
	s_ashr_i32 s18, s18, 2
	v_bfe_u32 v37, v231, s18, 1
	v_cmp_eq_u32_e32 vcc, 0, v37
	s_nop 1
	v_cndmask_b32_e32 v37, v36, v196, vcc
	v_cndmask_b32_e64 v44, v37, v36, s[0:1]
	s_waitcnt lgkmcnt(14)
	v_mfma_f32_32x32x16_f16 v[16:31], v[144:147], v[156:159], v[16:31]
	v_exp_f32_e32 v80, v80
	v_exp_f32_e32 v81, v81
	v_exp_f32_e32 v82, v82
	v_exp_f32_e32 v83, v83
	ds_read_b128 v[156:159], v44
	ds_read_b128 v[36:39], v44 offset:128
	s_waitcnt lgkmcnt(14)
	v_mfma_f32_32x32x16_f16 v[0:15], v[144:147], v[152:155], v[0:15]
	v_exp_f32_e32 v84, v84
	v_exp_f32_e32 v85, v85
	v_exp_f32_e32 v86, v86
	v_exp_f32_e32 v87, v87
	ds_read_b128 v[188:191], v44 offset:32
	ds_read_b128 v[198:201], v44 offset:160
	v_add_u32_e32 v144, s45, v232
	ds_read_b128 v[176:179], v144
	ds_read_b128 v[172:175], v144 offset:512
	s_waitcnt lgkmcnt(14)
	v_mfma_f32_32x32x16_f16 v[16:31], v[140:143], v[148:151], v[16:31]
	v_exp_f32_e32 v88, v88
	v_exp_f32_e32 v89, v89
	v_exp_f32_e32 v90, v90
	v_exp_f32_e32 v91, v91
	ds_read_b128 v[56:59], v44 offset:64
	ds_read_b128 v[40:43], v44 offset:192
	ds_read_b128 v[168:171], v144 offset:2048
	ds_read_b128 v[164:167], v144 offset:2560
	v_mfma_f32_32x32x16_f16 v[0:15], v[140:143], v[52:55], v[0:15]
	v_exp_f32_e32 v92, v92
	v_exp_f32_e32 v93, v93
	v_exp_f32_e32 v94, v94
	v_exp_f32_e32 v95, v95
	ds_read_b128 v[60:63], v44 offset:96
	ds_read_b128 v[44:47], v44 offset:224
	ds_read_b128 v[160:163], v144 offset:4096
	ds_read_b128 v[152:155], v144 offset:4608
	s_waitcnt lgkmcnt(14)
	v_mfma_f32_32x32x16_f16 v[16:31], v[136:139], v[48:51], v[16:31]
	v_exp_f32_e32 v64, v64
	v_exp_f32_e32 v65, v65
	v_exp_f32_e32 v66, v66
	v_exp_f32_e32 v67, v67
	s_waitcnt lgkmcnt(13)
	v_pk_add_f32 v[48:49], v[156:157], v[218:219] op_sel_hi:[1,0] neg_lo:[0,1] neg_hi:[0,1]
	v_pk_add_f32 v[50:51], v[158:159], v[218:219] op_sel_hi:[1,0] neg_lo:[0,1] neg_hi:[0,1]
	s_waitcnt lgkmcnt(11)
	v_pk_add_f32 v[52:53], v[188:189], v[218:219] op_sel_hi:[1,0] neg_lo:[0,1] neg_hi:[0,1]
	v_pk_add_f32 v[54:55], v[190:191], v[218:219] op_sel_hi:[1,0] neg_lo:[0,1] neg_hi:[0,1]
	s_waitcnt lgkmcnt(3)
	ds_read_b128 v[156:159], v144 offset:6144
	ds_read_b128 v[148:151], v144 offset:6656
	v_mfma_f32_32x32x16_f16 v[0:15], v[136:139], v[184:187], v[0:15]
	v_exp_f32_e32 v68, v68
	v_exp_f32_e32 v69, v69
	v_exp_f32_e32 v70, v70
	v_exp_f32_e32 v71, v71
	v_pk_add_f32 v[56:57], v[56:57], v[218:219] op_sel_hi:[1,0] neg_lo:[0,1] neg_hi:[0,1]
	v_pk_add_f32 v[58:59], v[58:59], v[218:219] op_sel_hi:[1,0] neg_lo:[0,1] neg_hi:[0,1]
	v_pk_add_f32 v[60:61], v[60:61], v[218:219] op_sel_hi:[1,0] neg_lo:[0,1] neg_hi:[0,1]
	v_pk_add_f32 v[62:63], v[62:63], v[218:219] op_sel_hi:[1,0] neg_lo:[0,1] neg_hi:[0,1]
	s_nop 0
	v_mfma_f32_32x32x16_f16 v[16:31], v[132:135], v[32:35], v[16:31]
	v_exp_f32_e32 v72, v72
	v_exp_f32_e32 v73, v73
	v_exp_f32_e32 v74, v74
	v_exp_f32_e32 v75, v75
	v_pk_add_f32 v[32:33], v[36:37], v[218:219] op_sel_hi:[1,0] neg_lo:[0,1] neg_hi:[0,1]
	v_pk_add_f32 v[34:35], v[38:39], v[218:219] op_sel_hi:[1,0] neg_lo:[0,1] neg_hi:[0,1]
	v_pk_add_f32 v[36:37], v[198:199], v[218:219] op_sel_hi:[1,0] neg_lo:[0,1] neg_hi:[0,1]
	v_pk_add_f32 v[38:39], v[200:201], v[218:219] op_sel_hi:[1,0] neg_lo:[0,1] neg_hi:[0,1]
	s_waitcnt lgkmcnt(4)
	v_mfma_f32_32x32x16_f16 v[0:15], v[132:135], v[180:183], v[0:15]
	v_exp_f32_e32 v76, v76
	v_exp_f32_e32 v77, v77
	v_exp_f32_e32 v78, v78
	v_exp_f32_e32 v79, v79
	v_pk_add_f32 v[40:41], v[40:41], v[218:219] op_sel_hi:[1,0] neg_lo:[0,1] neg_hi:[0,1]
	v_pk_add_f32 v[42:43], v[42:43], v[218:219] op_sel_hi:[1,0] neg_lo:[0,1] neg_hi:[0,1]
	v_pk_add_f32 v[44:45], v[44:45], v[218:219] op_sel_hi:[1,0] neg_lo:[0,1] neg_hi:[0,1]
	v_pk_add_f32 v[46:47], v[46:47], v[218:219] op_sel_hi:[1,0] neg_lo:[0,1] neg_hi:[0,1]
	s_nop 0
	s_waitcnt vmcnt(2) lgkmcnt(0)
	s_barrier
	s_setprio 0
	s_andn2_b64 vcc, exec, s[40:41]
	s_cbranch_vccnz .LBB0_487
	s_waitcnt lgkmcnt(0)
	ds_read_b128 v[180:183], v228 offset:49248
	ds_read_b128 v[184:187], v228 offset:49216
	ds_read_b128 v[188:191], v228 offset:49184
	ds_read_b128 v[198:201], v228 offset:49152
	s_waitcnt lgkmcnt(3)
	v_pk_mul_f32 v[30:31], v[30:31], v[182:183]
	s_waitcnt lgkmcnt(2)
	v_pk_mul_f32 v[26:27], v[26:27], v[186:187]
	s_waitcnt lgkmcnt(1)
	v_pk_mul_f32 v[22:23], v[22:23], v[190:191]
	s_waitcnt lgkmcnt(0)
	v_pk_mul_f32 v[18:19], v[18:19], v[200:201]
	v_pk_mul_f32 v[28:29], v[28:29], v[180:181]
	v_pk_mul_f32 v[24:25], v[24:25], v[184:185]
	v_pk_mul_f32 v[20:21], v[20:21], v[188:189]
	v_pk_mul_f32 v[16:17], v[16:17], v[198:199]
	v_pk_mul_f32 v[14:15], v[14:15], v[182:183]
	v_pk_mul_f32 v[10:11], v[10:11], v[186:187]
	v_pk_mul_f32 v[6:7], v[6:7], v[190:191]
	v_pk_mul_f32 v[2:3], v[2:3], v[200:201]
	v_pk_mul_f32 v[12:13], v[12:13], v[180:181]
	v_pk_mul_f32 v[8:9], v[8:9], v[184:185]
	v_pk_mul_f32 v[4:5], v[4:5], v[188:189]
	v_pk_mul_f32 v[0:1], v[0:1], v[198:199]

; __device__ __forceinline__ void cmask(f32x16& p0, f32x16& p1, int jb, int qrel, int hi) {
;     const float NEG = -INFINITY; int kb = 64 * jb + 4 * hi;
; #pragma unroll
;     for (int r = 0; r < 16; ++r) { int kv = kb + (r & 3) + 8 * (r >> 2); if (kv > qrel) p0[r] = NEG; if (kv + 32 > qrel) p1[r] = NEG; }
; }
.LBB0_625:
	v_add_u32_e32 v184, s40, v229
	ds_read_b64_tr_b16 v[180:181], v184 offset:24576
	ds_read_b64_tr_b16 v[182:183], v184 offset:25088
	s_waitcnt lgkmcnt(9)
	v_mfma_f32_32x32x16_f16 v[48:63], v[176:179], v[128:131], v[48:63]
	v_add_f32_e32 v132, v80, v81
	v_add_f32_e32 v132, v82, v132
	v_add_f32_e32 v132, v83, v132
	v_add_f32_e32 v132, v84, v132
	v_add_f32_e32 v132, v85, v132
	v_cvt_pk_f16_f32 v144, v80, v81
	v_cvt_pk_f16_f32 v145, v82, v83
	ds_read_b64_tr_b16 v[176:177], v184 offset:28672
	ds_read_b64_tr_b16 v[178:179], v184 offset:29184
	s_waitcnt lgkmcnt(10)
	v_mfma_f32_32x32x16_f16 v[32:47], v[172:175], v[128:131], v[32:47]
	v_add_f32_e32 v80, v86, v132
	v_add_f32_e32 v80, v87, v80
	v_add_f32_e32 v80, v88, v80
	v_add_f32_e32 v80, v89, v80
	v_cvt_pk_f16_f32 v146, v84, v85
	v_cvt_pk_f16_f32 v147, v86, v87
	ds_read_b64_tr_b16 v[172:173], v184 offset:25600
	ds_read_b64_tr_b16 v[174:175], v184 offset:26112
	s_waitcnt lgkmcnt(11)
	v_mfma_f32_32x32x16_f16 v[48:63], v[168:171], v[124:127], v[48:63]
	v_add_f32_e32 v80, v90, v80
	v_add_f32_e32 v80, v91, v80
	v_add_f32_e32 v80, v92, v80
	v_add_f32_e32 v80, v93, v80
	v_cvt_pk_f16_f32 v140, v88, v89
	v_cvt_pk_f16_f32 v141, v90, v91
	ds_read_b64_tr_b16 v[84:85], v184 offset:29696
	ds_read_b64_tr_b16 v[86:87], v184 offset:30208
	s_waitcnt lgkmcnt(12)
	v_mfma_f32_32x32x16_f16 v[32:47], v[164:167], v[124:127], v[32:47]
	v_add_f32_e32 v80, v94, v80
	v_add_f32_e32 v80, v95, v80
	v_add_f32_e32 v80, v64, v80
	v_add_f32_e32 v88, v65, v80
	v_cvt_pk_f16_f32 v142, v92, v93
	v_cvt_pk_f16_f32 v143, v94, v95
	ds_read_b64_tr_b16 v[80:81], v184 offset:26624
	ds_read_b64_tr_b16 v[82:83], v184 offset:27136
	s_waitcnt lgkmcnt(13)
	v_mfma_f32_32x32x16_f16 v[48:63], v[160:163], v[120:123], v[48:63]
	v_add_f32_e32 v88, v66, v88
	v_add_f32_e32 v88, v67, v88
	v_add_f32_e32 v88, v68, v88
	v_add_f32_e32 v88, v69, v88
	v_cvt_pk_f16_f32 v136, v64, v65
	v_cvt_pk_f16_f32 v137, v66, v67
	ds_read_b64_tr_b16 v[160:161], v184 offset:30720
	ds_read_b64_tr_b16 v[162:163], v184 offset:31232
	s_waitcnt lgkmcnt(14)
	v_mfma_f32_32x32x16_f16 v[32:47], v[152:155], v[120:123], v[32:47]
	v_add_f32_e32 v64, v70, v88
	v_add_f32_e32 v64, v71, v64
	v_add_f32_e32 v64, v72, v64
	v_add_f32_e32 v88, v73, v64
	v_cvt_pk_f16_f32 v138, v68, v69
	v_cvt_pk_f16_f32 v139, v70, v71
	ds_read_b64_tr_b16 v[64:65], v184 offset:27648
	ds_read_b64_tr_b16 v[66:67], v184 offset:28160
	s_waitcnt lgkmcnt(14)
	v_mfma_f32_32x32x16_f16 v[48:63], v[156:159], v[116:119], v[48:63]
	v_add_f32_e32 v68, v74, v88
	v_add_f32_e32 v68, v75, v68
	v_add_f32_e32 v68, v76, v68
	v_add_f32_e32 v68, v77, v68
	v_cvt_pk_f16_f32 v132, v72, v73
	v_cvt_pk_f16_f32 v133, v74, v75
	ds_read_b64_tr_b16 v[152:153], v184 offset:31744
	ds_read_b64_tr_b16 v[154:155], v184 offset:32256
	v_mfma_f32_32x32x16_f16 v[32:47], v[148:151], v[116:119], v[32:47]
	v_add_f32_e32 v68, v78, v68
	v_add_f32_e32 v68, v79, v68
	v_add_f32_e32 v68, 0, v68
	v_cvt_pk_f16_f32 v134, v76, v77
	v_cvt_pk_f16_f32 v135, v78, v79
	v_lshl_add_u64 v[70:71], v[194:195], 0, s[30:31]
	s_add_i32 s11, s69, s90
	s_mov_b32 s18, m0
	s_mov_b32 m0, s11
	s_nop 0
	global_load_lds_dwordx4 v[70:71], off
	s_mov_b32 m0, s18
	s_add_i32 s18, s26, s45
	s_add_i32 s37, s26, s19
	s_add_i32 s11, s18, 1
	s_add_i32 s66, s37, 1
	s_cmp_lt_u32 s45, 3
	s_cselect_b64 s[40:41], -1, 0
	s_and_b64 s[50:51], s[40:41], exec
	s_cselect_b32 s11, s11, s66
	v_mad_i64_i32 v[70:71], s[50:51], s11, v249, v[216:217]
	s_add_i32 s50, s68, s10
	s_mov_b32 s51, m0
	s_mov_b32 m0, s50
	s_nop 0
	global_load_lds_dwordx4 v[70:71], off
	s_mov_b32 m0, s51
	s_cmp_gt_u32 s45, 3
	s_cbranch_scc1 .LBB0_627
	s_mov_b64 s[100:101], exec
	v_sub_u32_e32 v69, v215, v196
	v_add_u32_e32 v69, 32, v69
	v_cmpx_gt_i32_e32 59, v69
	s_nop 3
	s_cbranch_execz .Lmaskx_done_4
	s_setprio 1
	v_mov_b32_e32 v47, v248
	v_cmpx_gt_i32_e32 58, v69
	v_mov_b32_e32 v46, v248
	v_cmpx_gt_i32_e32 57, v69
	v_mov_b32_e32 v45, v248
	v_cmpx_gt_i32_e32 56, v69
	v_mov_b32_e32 v44, v248
	v_cmpx_gt_i32_e32 51, v69
	v_mov_b32_e32 v43, v248
	v_cmpx_gt_i32_e32 50, v69
	v_mov_b32_e32 v42, v248
	v_cmpx_gt_i32_e32 49, v69
	v_mov_b32_e32 v41, v248
	v_cmpx_gt_i32_e32 48, v69
	v_mov_b32_e32 v40, v248
	v_cmpx_gt_i32_e32 43, v69
	v_mov_b32_e32 v39, v248
	v_cmpx_gt_i32_e32 42, v69
	v_mov_b32_e32 v38, v248
	v_cmpx_gt_i32_e32 41, v69
	v_mov_b32_e32 v37, v248
	v_cmpx_gt_i32_e32 40, v69
	v_mov_b32_e32 v36, v248
	v_cmpx_gt_i32_e32 35, v69
	v_mov_b32_e32 v35, v248
	v_cmpx_gt_i32_e32 34, v69
	v_mov_b32_e32 v34, v248
	v_cmpx_gt_i32_e32 33, v69
	v_mov_b32_e32 v33, v248
	v_cmpx_gt_i32_e32 32, v69
	v_mov_b32_e32 v32, v248
	v_cmpx_gt_i32_e32 27, v69
	v_mov_b32_e32 v63, v248
	v_cmpx_gt_i32_e32 26, v69
	v_mov_b32_e32 v62, v248
	v_cmpx_gt_i32_e32 25, v69
	v_mov_b32_e32 v61, v248
	v_cmpx_gt_i32_e32 24, v69
	v_mov_b32_e32 v60, v248
	v_cmpx_gt_i32_e32 19, v69
	v_mov_b32_e32 v59, v248
	v_cmpx_gt_i32_e32 18, v69
	v_mov_b32_e32 v58, v248
	v_cmpx_gt_i32_e32 17, v69
	v_mov_b32_e32 v57, v248
	v_cmpx_gt_i32_e32 16, v69
	v_mov_b32_e32 v56, v248
	v_cmpx_gt_i32_e32 11, v69
	v_mov_b32_e32 v55, v248
	v_cmpx_gt_i32_e32 10, v69
	v_mov_b32_e32 v54, v248
	v_cmpx_gt_i32_e32 9, v69
	v_mov_b32_e32 v53, v248
	v_cmpx_gt_i32_e32 8, v69
	v_mov_b32_e32 v52, v248
	v_cmpx_gt_i32_e32 3, v69
	v_mov_b32_e32 v51, v248
	v_cmpx_gt_i32_e32 2, v69
	v_mov_b32_e32 v50, v248
	v_cmpx_gt_i32_e32 1, v69
	v_mov_b32_e32 v49, v248
	v_cmpx_gt_i32_e32 0, v69
	v_mov_b32_e32 v48, v248

; #define WAIT_BAR(N) asm volatile("s_waitcnt vmcnt(" #N ") lgkmcnt(0)\n\ts_barrier" ::: "memory")
; #define RESC() do { if (resc) { asm volatile("s_waitcnt lgkmcnt(0)" ::: "memory"); \
;       _Pragma("unroll") for (int d_ = 0; d_ < 2; ++d_) _Pragma("unroll") for (int r = 0; r < 16; ++r) o[d_][r] *= wsf[crow(r, hi)]; } } while (0)
; #define ROT() do { sl_prev = sl_cur; sl_cur = sl_next; sl_next = (sl_next == (NSLOT - 1) * SLOTB) ? 0 : sl_next + SLOTB; } while (0)
; template <bool MOBA, int THRL> ...
;     ...
;     bool resc = false;
;     ...
;     int t = 1;
;     ...
;     for (; t + 5 < NT; t += 2) {
;         STEP(pB0, pB1, pA0, pA1, t, true, true, true);       WAIT_BAR(2); RESC(); ROT();
.LBB0_628:
	s_waitcnt lgkmcnt(14)
	v_mfma_f32_32x32x16_f16 v[16:31], v[144:147], v[180:183], v[16:31]
	v_exp_f32_e32 v48, v48
	v_exp_f32_e32 v49, v49
	v_exp_f32_e32 v50, v50
	v_exp_f32_e32 v51, v51
	v_lshl_add_u32 v76, s11, 8, v232
	ds_read_b128 v[156:159], v76
	ds_read_b128 v[68:71], v76 offset:128
	s_waitcnt lgkmcnt(14)
	v_mfma_f32_32x32x16_f16 v[0:15], v[144:147], v[176:179], v[0:15]
	v_exp_f32_e32 v52, v52
	v_exp_f32_e32 v53, v53
	v_exp_f32_e32 v54, v54
	v_exp_f32_e32 v55, v55
	ds_read_b128 v[168:171], v76 offset:32
	ds_read_b128 v[198:201], v76 offset:160
	v_add_u32_e32 v144, s68, v230
	ds_read_b128 v[188:191], v144
	ds_read_b128 v[148:151], v144 offset:512
	s_waitcnt lgkmcnt(14)
	v_mfma_f32_32x32x16_f16 v[16:31], v[140:143], v[172:175], v[16:31]
	v_exp_f32_e32 v56, v56
	v_exp_f32_e32 v57, v57
	v_exp_f32_e32 v58, v58
	v_exp_f32_e32 v59, v59
	ds_read_b128 v[88:91], v76 offset:64
	ds_read_b128 v[72:75], v76 offset:192
	ds_read_b128 v[184:187], v144 offset:2048
	ds_read_b128 v[172:175], v144 offset:2560
	v_mfma_f32_32x32x16_f16 v[0:15], v[140:143], v[84:87], v[0:15]
	v_exp_f32_e32 v60, v60
	v_exp_f32_e32 v61, v61
	v_exp_f32_e32 v62, v62
	v_exp_f32_e32 v63, v63
	ds_read_b128 v[92:95], v76 offset:96
	ds_read_b128 v[76:79], v76 offset:224
	ds_read_b128 v[176:179], v144 offset:4096
	ds_read_b128 v[164:167], v144 offset:4608
	s_waitcnt lgkmcnt(14)
	v_mfma_f32_32x32x16_f16 v[16:31], v[136:139], v[80:83], v[16:31]
	v_exp_f32_e32 v32, v32
	v_exp_f32_e32 v33, v33
	v_exp_f32_e32 v34, v34
	v_exp_f32_e32 v35, v35
	s_waitcnt lgkmcnt(13)
	v_pk_add_f32 v[80:81], v[156:157], v[218:219] op_sel_hi:[1,0] neg_lo:[0,1] neg_hi:[0,1]
	v_pk_add_f32 v[82:83], v[158:159], v[218:219] op_sel_hi:[1,0] neg_lo:[0,1] neg_hi:[0,1]
	s_waitcnt lgkmcnt(11)
	v_pk_add_f32 v[84:85], v[168:169], v[218:219] op_sel_hi:[1,0] neg_lo:[0,1] neg_hi:[0,1]
	v_pk_add_f32 v[86:87], v[170:171], v[218:219] op_sel_hi:[1,0] neg_lo:[0,1] neg_hi:[0,1]
	s_waitcnt lgkmcnt(3)
	ds_read_b128 v[180:183], v144 offset:6144
	ds_read_b128 v[168:171], v144 offset:6656
	v_mfma_f32_32x32x16_f16 v[0:15], v[136:139], v[160:163], v[0:15]
	v_exp_f32_e32 v36, v36
	v_exp_f32_e32 v37, v37
	v_exp_f32_e32 v38, v38
	v_exp_f32_e32 v39, v39
	v_pk_add_f32 v[88:89], v[88:89], v[218:219] op_sel_hi:[1,0] neg_lo:[0,1] neg_hi:[0,1]
	v_pk_add_f32 v[90:91], v[90:91], v[218:219] op_sel_hi:[1,0] neg_lo:[0,1] neg_hi:[0,1]
	v_pk_add_f32 v[92:93], v[92:93], v[218:219] op_sel_hi:[1,0] neg_lo:[0,1] neg_hi:[0,1]
	v_pk_add_f32 v[94:95], v[94:95], v[218:219] op_sel_hi:[1,0] neg_lo:[0,1] neg_hi:[0,1]
	s_nop 0
	v_mfma_f32_32x32x16_f16 v[16:31], v[132:135], v[64:67], v[16:31]
	v_exp_f32_e32 v40, v40
	v_exp_f32_e32 v41, v41
	v_exp_f32_e32 v42, v42
	v_exp_f32_e32 v43, v43
	v_pk_add_f32 v[64:65], v[68:69], v[218:219] op_sel_hi:[1,0] neg_lo:[0,1] neg_hi:[0,1]
	v_pk_add_f32 v[66:67], v[70:71], v[218:219] op_sel_hi:[1,0] neg_lo:[0,1] neg_hi:[0,1]
	v_pk_add_f32 v[68:69], v[198:199], v[218:219] op_sel_hi:[1,0] neg_lo:[0,1] neg_hi:[0,1]
	v_pk_add_f32 v[70:71], v[200:201], v[218:219] op_sel_hi:[1,0] neg_lo:[0,1] neg_hi:[0,1]
	s_waitcnt lgkmcnt(4)
	v_mfma_f32_32x32x16_f16 v[0:15], v[132:135], v[152:155], v[0:15]
	v_exp_f32_e32 v44, v44
	v_exp_f32_e32 v45, v45
	v_exp_f32_e32 v46, v46
	v_exp_f32_e32 v47, v47
	v_pk_add_f32 v[72:73], v[72:73], v[218:219] op_sel_hi:[1,0] neg_lo:[0,1] neg_hi:[0,1]
	v_pk_add_f32 v[74:75], v[74:75], v[218:219] op_sel_hi:[1,0] neg_lo:[0,1] neg_hi:[0,1]
	v_pk_add_f32 v[76:77], v[76:77], v[218:219] op_sel_hi:[1,0] neg_lo:[0,1] neg_hi:[0,1]
	v_pk_add_f32 v[78:79], v[78:79], v[218:219] op_sel_hi:[1,0] neg_lo:[0,1] neg_hi:[0,1]
	s_nop 0
	s_waitcnt vmcnt(2) lgkmcnt(0)
	s_barrier
	s_setprio 0
	s_andn2_b64 vcc, exec, s[50:51]
	s_cbranch_vccnz .LBB0_630
	s_waitcnt lgkmcnt(0)
	ds_read_b128 v[152:155], v227 offset:49248
	ds_read_b128 v[156:159], v227 offset:49216
	ds_read_b128 v[160:163], v227 offset:49184
	ds_read_b128 v[198:201], v227 offset:49152
	s_waitcnt lgkmcnt(3)
	v_pk_mul_f32 v[30:31], v[30:31], v[154:155]
	s_waitcnt lgkmcnt(2)
	v_pk_mul_f32 v[26:27], v[26:27], v[158:159]
	s_waitcnt lgkmcnt(1)
	v_pk_mul_f32 v[22:23], v[22:23], v[162:163]
	s_waitcnt lgkmcnt(0)
	v_pk_mul_f32 v[18:19], v[18:19], v[200:201]
	v_pk_mul_f32 v[28:29], v[28:29], v[152:153]
	v_pk_mul_f32 v[24:25], v[24:25], v[156:157]
	v_pk_mul_f32 v[20:21], v[20:21], v[160:161]
	v_pk_mul_f32 v[16:17], v[16:17], v[198:199]
	v_pk_mul_f32 v[14:15], v[14:15], v[154:155]
	v_pk_mul_f32 v[10:11], v[10:11], v[158:159]
	v_pk_mul_f32 v[6:7], v[6:7], v[162:163]
	v_pk_mul_f32 v[2:3], v[2:3], v[200:201]
	v_pk_mul_f32 v[12:13], v[12:13], v[152:153]
	v_pk_mul_f32 v[8:9], v[8:9], v[156:157]
	v_pk_mul_f32 v[4:5], v[4:5], v[160:161]
	v_pk_mul_f32 v[0:1], v[0:1], v[198:199]
; __device__ __forceinline__ void cmask(f32x16& p0, f32x16& p1, int jb, int qrel, int hi) {
;     const float NEG = -INFINITY; int kb = 64 * jb + 4 * hi;
; #pragma unroll
;     for (int r = 0; r < 16; ++r) { int kv = kb + (r & 3) + 8 * (r >> 2); if (kv > qrel) p0[r] = NEG; if (kv + 32 > qrel) p1[r] = NEG; }
; }
.LBB0_630:
	s_add_i32 s11, s68, 0x2000
	s_cmpk_lg_i32 s68, 0x4000
	s_cselect_b32 s11, s11, 0
	v_add_u32_e32 v160, s69, v229
	ds_read_b64_tr_b16 v[156:157], v160 offset:24576
	ds_read_b64_tr_b16 v[158:159], v160 offset:25088
	v_mfma_f32_32x32x16_f16 v[80:95], v[188:191], v[128:131], v[80:95]
	v_add_f32_e32 v132, v48, v49
	v_add_f32_e32 v132, v50, v132
	v_add_f32_e32 v132, v51, v132
	v_add_f32_e32 v132, v52, v132
	v_add_f32_e32 v132, v53, v132
	v_cvt_pk_f16_f32 v144, v48, v49
	v_cvt_pk_f16_f32 v145, v50, v51
	ds_read_b64_tr_b16 v[152:153], v160 offset:28672
	ds_read_b64_tr_b16 v[154:155], v160 offset:29184
	v_mfma_f32_32x32x16_f16 v[64:79], v[148:151], v[128:131], v[64:79]
	v_add_f32_e32 v48, v54, v132
	v_add_f32_e32 v48, v55, v48
	v_add_f32_e32 v48, v56, v48
	v_add_f32_e32 v48, v57, v48
	v_cvt_pk_f16_f32 v146, v52, v53
	v_cvt_pk_f16_f32 v147, v54, v55
	ds_read_b64_tr_b16 v[148:149], v160 offset:25600
	ds_read_b64_tr_b16 v[150:151], v160 offset:26112
	v_mfma_f32_32x32x16_f16 v[80:95], v[184:187], v[124:127], v[80:95]
	v_add_f32_e32 v48, v58, v48
	v_add_f32_e32 v48, v59, v48
	v_add_f32_e32 v48, v60, v48
	v_add_f32_e32 v48, v61, v48
	v_cvt_pk_f16_f32 v140, v56, v57
	v_cvt_pk_f16_f32 v141, v58, v59
	ds_read_b64_tr_b16 v[52:53], v160 offset:29696
	ds_read_b64_tr_b16 v[54:55], v160 offset:30208
	v_mfma_f32_32x32x16_f16 v[64:79], v[172:175], v[124:127], v[64:79]
	v_add_f32_e32 v48, v62, v48
	v_add_f32_e32 v48, v63, v48
	v_add_f32_e32 v48, v32, v48
	v_add_f32_e32 v56, v33, v48
	v_cvt_pk_f16_f32 v142, v60, v61
	v_cvt_pk_f16_f32 v143, v62, v63
	ds_read_b64_tr_b16 v[48:49], v160 offset:26624
	ds_read_b64_tr_b16 v[50:51], v160 offset:27136
	s_waitcnt lgkmcnt(13)
	v_mfma_f32_32x32x16_f16 v[80:95], v[176:179], v[120:123], v[80:95]
	v_add_f32_e32 v56, v34, v56
	v_add_f32_e32 v56, v35, v56
	v_add_f32_e32 v56, v36, v56
	v_add_f32_e32 v56, v37, v56
	v_cvt_pk_f16_f32 v136, v32, v33
	v_cvt_pk_f16_f32 v137, v34, v35
	ds_read_b64_tr_b16 v[184:185], v160 offset:30720
	ds_read_b64_tr_b16 v[186:187], v160 offset:31232
	s_waitcnt lgkmcnt(14)
	v_mfma_f32_32x32x16_f16 v[64:79], v[164:167], v[120:123], v[64:79]
	v_add_f32_e32 v32, v38, v56
	v_add_f32_e32 v32, v39, v32
	v_add_f32_e32 v32, v40, v32
	v_add_f32_e32 v56, v41, v32
	v_cvt_pk_f16_f32 v138, v36, v37
	v_cvt_pk_f16_f32 v139, v38, v39
	ds_read_b64_tr_b16 v[32:33], v160 offset:27648
	ds_read_b64_tr_b16 v[34:35], v160 offset:28160
	s_waitcnt lgkmcnt(14)
	v_mfma_f32_32x32x16_f16 v[80:95], v[180:183], v[116:119], v[80:95]
	v_add_f32_e32 v36, v42, v56
	v_add_f32_e32 v36, v43, v36
	v_add_f32_e32 v36, v44, v36
	v_add_f32_e32 v36, v45, v36
	v_cvt_pk_f16_f32 v132, v40, v41
	v_cvt_pk_f16_f32 v133, v42, v43
	ds_read_b64_tr_b16 v[180:181], v160 offset:31744
	ds_read_b64_tr_b16 v[182:183], v160 offset:32256
	v_mfma_f32_32x32x16_f16 v[64:79], v[168:171], v[116:119], v[64:79]
	v_add_f32_e32 v36, v46, v36
	v_add_f32_e32 v36, v47, v36
	v_add_f32_e32 v36, 0, v36
	v_cvt_pk_f16_f32 v134, v44, v45
	v_cvt_pk_f16_f32 v135, v46, v47
	s_add_i32 s50, s68, s90
	s_add_i32 s18, s18, 2
	s_cmp_lt_u32 s45, 2
	s_mov_b32 s51, m0
	s_mov_b32 m0, s50
	s_nop 0
	global_load_lds_dwordx4 v[194:195], off
	s_mov_b32 m0, s51
	s_cselect_b32 s18, s18, s37
	v_mad_i64_i32 v[38:39], s[50:51], s18, v249, v[216:217]
	s_add_i32 s37, s11, s10
	s_mov_b32 s50, m0
	s_mov_b32 m0, s37
	s_nop 0
	global_load_lds_dwordx4 v[38:39], off
	s_mov_b32 m0, s50
	s_andn2_b64 vcc, exec, s[40:41]
	s_cbranch_vccnz .LBB0_632
	s_mov_b64 s[100:101], exec
	v_sub_u32_e32 v38, v215, v196
	v_add_u32_e32 v38, 0xffffffe0, v38
	v_cmpx_gt_i32_e32 59, v38
	s_nop 3
	s_cbranch_execz .Lmaskx_done_3
	s_setprio 1
	v_mov_b32_e32 v79, v248
	v_cmpx_gt_i32_e32 58, v38
	v_mov_b32_e32 v78, v248
	v_cmpx_gt_i32_e32 57, v38
	v_mov_b32_e32 v77, v248
	v_cmpx_gt_i32_e32 56, v38
	v_mov_b32_e32 v76, v248
	v_cmpx_gt_i32_e32 51, v38
	v_mov_b32_e32 v75, v248
	v_cmpx_gt_i32_e32 50, v38
	v_mov_b32_e32 v74, v248
	v_cmpx_gt_i32_e32 49, v38
	v_mov_b32_e32 v73, v248
	v_cmpx_gt_i32_e32 48, v38
	v_mov_b32_e32 v72, v248
	v_cmpx_gt_i32_e32 43, v38
	v_mov_b32_e32 v71, v248
	v_cmpx_gt_i32_e32 42, v38
	v_mov_b32_e32 v70, v248
	v_cmpx_gt_i32_e32 41, v38
	v_mov_b32_e32 v69, v248
	v_cmpx_gt_i32_e32 40, v38
	v_mov_b32_e32 v68, v248
	v_cmpx_gt_i32_e32 35, v38
	v_mov_b32_e32 v67, v248
	v_cmpx_gt_i32_e32 34, v38
	v_mov_b32_e32 v66, v248
	v_cmpx_gt_i32_e32 33, v38
	v_mov_b32_e32 v65, v248
	v_cmpx_gt_i32_e32 32, v38
	v_mov_b32_e32 v64, v248
	v_cmpx_gt_i32_e32 27, v38
	v_mov_b32_e32 v95, v248
	v_cmpx_gt_i32_e32 26, v38
	v_mov_b32_e32 v94, v248
	v_cmpx_gt_i32_e32 25, v38
	v_mov_b32_e32 v93, v248
	v_cmpx_gt_i32_e32 24, v38
	v_mov_b32_e32 v92, v248
	v_cmpx_gt_i32_e32 19, v38
	v_mov_b32_e32 v91, v248
	v_cmpx_gt_i32_e32 18, v38
	v_mov_b32_e32 v90, v248
	v_cmpx_gt_i32_e32 17, v38
	v_mov_b32_e32 v89, v248
	v_cmpx_gt_i32_e32 16, v38
	v_mov_b32_e32 v88, v248
	v_cmpx_gt_i32_e32 11, v38
	v_mov_b32_e32 v87, v248
	v_cmpx_gt_i32_e32 10, v38
	v_mov_b32_e32 v86, v248
	v_cmpx_gt_i32_e32 9, v38
	v_mov_b32_e32 v85, v248
	v_cmpx_gt_i32_e32 8, v38
	v_mov_b32_e32 v84, v248
	v_cmpx_gt_i32_e32 3, v38
	v_mov_b32_e32 v83, v248
	v_cmpx_gt_i32_e32 2, v38
	v_mov_b32_e32 v82, v248
	v_cmpx_gt_i32_e32 1, v38
	v_mov_b32_e32 v81, v248
	v_cmpx_gt_i32_e32 0, v38
	v_mov_b32_e32 v80, v248

; #define WAIT_BAR(N) asm volatile("s_waitcnt vmcnt(" #N ") lgkmcnt(0)\n\ts_barrier" ::: "memory")
; #define RESC() do { if (resc) { asm volatile("s_waitcnt lgkmcnt(0)" ::: "memory"); \
;       _Pragma("unroll") for (int d_ = 0; d_ < 2; ++d_) _Pragma("unroll") for (int r = 0; r < 16; ++r) o[d_][r] *= wsf[crow(r, hi)]; } } while (0)
; #define ROT() do { sl_prev = sl_cur; sl_cur = sl_next; sl_next = (sl_next == (NSLOT - 1) * SLOTB) ? 0 : sl_next + SLOTB; } while (0)
; template <bool MOBA, int THRL> ...
;     ...
;     bool resc = false;
;     ...
;     int t = 1;
;     ...
;     for (; t + 5 < NT; t += 2) {
;         STEP(pB0, pB1, pA0, pA1, t, true, true, true);       WAIT_BAR(2); RESC(); ROT();
.LBB0_633:
	s_waitcnt lgkmcnt(14)
	v_mfma_f32_32x32x16_f16 v[16:31], v[144:147], v[156:159], v[16:31]
	v_exp_f32_e32 v80, v80
	v_exp_f32_e32 v81, v81
	v_exp_f32_e32 v82, v82
	v_exp_f32_e32 v83, v83
	v_lshl_add_u32 v44, s18, 8, v232
	ds_read_b128 v[156:159], v44
	ds_read_b128 v[36:39], v44 offset:128
	s_waitcnt lgkmcnt(14)
	v_mfma_f32_32x32x16_f16 v[0:15], v[144:147], v[152:155], v[0:15]
	v_exp_f32_e32 v84, v84
	v_exp_f32_e32 v85, v85
	v_exp_f32_e32 v86, v86
	v_exp_f32_e32 v87, v87
	ds_read_b128 v[188:191], v44 offset:32
	ds_read_b128 v[198:201], v44 offset:160
	v_add_u32_e32 v144, s11, v230
	ds_read_b128 v[176:179], v144
	ds_read_b128 v[172:175], v144 offset:512
	s_waitcnt lgkmcnt(14)
	v_mfma_f32_32x32x16_f16 v[16:31], v[140:143], v[148:151], v[16:31]
	v_exp_f32_e32 v88, v88
	v_exp_f32_e32 v89, v89
	v_exp_f32_e32 v90, v90
	v_exp_f32_e32 v91, v91
	ds_read_b128 v[56:59], v44 offset:64
	ds_read_b128 v[40:43], v44 offset:192
	ds_read_b128 v[168:171], v144 offset:2048
	ds_read_b128 v[164:167], v144 offset:2560
	v_mfma_f32_32x32x16_f16 v[0:15], v[140:143], v[52:55], v[0:15]
	v_exp_f32_e32 v92, v92
	v_exp_f32_e32 v93, v93
	v_exp_f32_e32 v94, v94
	v_exp_f32_e32 v95, v95
	ds_read_b128 v[60:63], v44 offset:96
	ds_read_b128 v[44:47], v44 offset:224
	ds_read_b128 v[160:163], v144 offset:4096
	ds_read_b128 v[152:155], v144 offset:4608
	s_waitcnt lgkmcnt(14)
	v_mfma_f32_32x32x16_f16 v[16:31], v[136:139], v[48:51], v[16:31]
	v_exp_f32_e32 v64, v64
	v_exp_f32_e32 v65, v65
	v_exp_f32_e32 v66, v66
	v_exp_f32_e32 v67, v67
	s_waitcnt lgkmcnt(13)
	v_pk_add_f32 v[48:49], v[156:157], v[218:219] op_sel_hi:[1,0] neg_lo:[0,1] neg_hi:[0,1]
	v_pk_add_f32 v[50:51], v[158:159], v[218:219] op_sel_hi:[1,0] neg_lo:[0,1] neg_hi:[0,1]
	s_waitcnt lgkmcnt(11)
	v_pk_add_f32 v[52:53], v[188:189], v[218:219] op_sel_hi:[1,0] neg_lo:[0,1] neg_hi:[0,1]
	v_pk_add_f32 v[54:55], v[190:191], v[218:219] op_sel_hi:[1,0] neg_lo:[0,1] neg_hi:[0,1]
	s_waitcnt lgkmcnt(3)
	ds_read_b128 v[156:159], v144 offset:6144
	ds_read_b128 v[148:151], v144 offset:6656
	v_mfma_f32_32x32x16_f16 v[0:15], v[136:139], v[184:187], v[0:15]
	v_exp_f32_e32 v68, v68
	v_exp_f32_e32 v69, v69
	v_exp_f32_e32 v70, v70
	v_exp_f32_e32 v71, v71
	v_pk_add_f32 v[56:57], v[56:57], v[218:219] op_sel_hi:[1,0] neg_lo:[0,1] neg_hi:[0,1]
	v_pk_add_f32 v[58:59], v[58:59], v[218:219] op_sel_hi:[1,0] neg_lo:[0,1] neg_hi:[0,1]
	v_pk_add_f32 v[60:61], v[60:61], v[218:219] op_sel_hi:[1,0] neg_lo:[0,1] neg_hi:[0,1]
	v_pk_add_f32 v[62:63], v[62:63], v[218:219] op_sel_hi:[1,0] neg_lo:[0,1] neg_hi:[0,1]
	s_nop 0
	v_mfma_f32_32x32x16_f16 v[16:31], v[132:135], v[32:35], v[16:31]
	v_exp_f32_e32 v72, v72
	v_exp_f32_e32 v73, v73
	v_exp_f32_e32 v74, v74
	v_exp_f32_e32 v75, v75
	v_pk_add_f32 v[32:33], v[36:37], v[218:219] op_sel_hi:[1,0] neg_lo:[0,1] neg_hi:[0,1]
	v_pk_add_f32 v[34:35], v[38:39], v[218:219] op_sel_hi:[1,0] neg_lo:[0,1] neg_hi:[0,1]
	v_pk_add_f32 v[36:37], v[198:199], v[218:219] op_sel_hi:[1,0] neg_lo:[0,1] neg_hi:[0,1]
	v_pk_add_f32 v[38:39], v[200:201], v[218:219] op_sel_hi:[1,0] neg_lo:[0,1] neg_hi:[0,1]
	s_waitcnt lgkmcnt(4)
	v_mfma_f32_32x32x16_f16 v[0:15], v[132:135], v[180:183], v[0:15]
	v_exp_f32_e32 v76, v76
	v_exp_f32_e32 v77, v77
	v_exp_f32_e32 v78, v78
	v_exp_f32_e32 v79, v79
	v_pk_add_f32 v[40:41], v[40:41], v[218:219] op_sel_hi:[1,0] neg_lo:[0,1] neg_hi:[0,1]
	v_pk_add_f32 v[42:43], v[42:43], v[218:219] op_sel_hi:[1,0] neg_lo:[0,1] neg_hi:[0,1]
	v_pk_add_f32 v[44:45], v[44:45], v[218:219] op_sel_hi:[1,0] neg_lo:[0,1] neg_hi:[0,1]
	v_pk_add_f32 v[46:47], v[46:47], v[218:219] op_sel_hi:[1,0] neg_lo:[0,1] neg_hi:[0,1]
	s_nop 0
	s_waitcnt vmcnt(2) lgkmcnt(0)
	s_barrier
	s_setprio 0
	s_andn2_b64 vcc, exec, s[40:41]
	s_cbranch_vccnz .LBB0_635
	s_waitcnt lgkmcnt(0)
	ds_read_b128 v[180:183], v227 offset:49248
	ds_read_b128 v[184:187], v227 offset:49216
	ds_read_b128 v[188:191], v227 offset:49184
	ds_read_b128 v[198:201], v227 offset:49152
	s_waitcnt lgkmcnt(3)
	v_pk_mul_f32 v[30:31], v[30:31], v[182:183]
	s_waitcnt lgkmcnt(2)
	v_pk_mul_f32 v[26:27], v[26:27], v[186:187]
	s_waitcnt lgkmcnt(1)
	v_pk_mul_f32 v[22:23], v[22:23], v[190:191]
	s_waitcnt lgkmcnt(0)
	v_pk_mul_f32 v[18:19], v[18:19], v[200:201]
	v_pk_mul_f32 v[28:29], v[28:29], v[180:181]
	v_pk_mul_f32 v[24:25], v[24:25], v[184:185]
	v_pk_mul_f32 v[20:21], v[20:21], v[188:189]
	v_pk_mul_f32 v[16:17], v[16:17], v[198:199]
	v_pk_mul_f32 v[14:15], v[14:15], v[182:183]
	v_pk_mul_f32 v[10:11], v[10:11], v[186:187]
	v_pk_mul_f32 v[6:7], v[6:7], v[190:191]
	v_pk_mul_f32 v[2:3], v[2:3], v[200:201]
	v_pk_mul_f32 v[12:13], v[12:13], v[180:181]
	v_pk_mul_f32 v[8:9], v[8:9], v[184:185]
	v_pk_mul_f32 v[4:5], v[4:5], v[188:189]
	v_pk_mul_f32 v[0:1], v[0:1], v[198:199]
